# baseline (speedup 1.0000x reference)
_Z15attn_varlen_fwdPKfS0_S0_PKiPf5Sched:
	s_load_dwordx2 s[4:5], s[0:1], 0x18
	s_and_b32 s3, s2, 0x78
	s_load_dword s6, s[0:1], s3 offset:0x28
	s_load_dwordx2 s[72:73], s[0:1], 0x20
	s_load_dwordx4 s[68:71], s[0:1], 0x0
	s_load_dwordx2 s[74:75], s[0:1], 0x10
	s_add_u32 s3, s0, s3
	v_readfirstlane_b32 s8, v0
	s_waitcnt lgkmcnt(0)
	s_mov_b64 s[10:11], s[4:5]
	v_writelane_b32 v255, s4, 0
	s_nop 1
	v_writelane_b32 v255, s5, 1
	s_addc_u32 s5, s1, 0
	s_add_u32 s4, s3, 40
	s_addc_u32 s5, s5, 0
	s_and_b32 s9, s6, 0xff
	s_cmpk_lg_i32 s9, 0xff
	s_cselect_b64 s[6:7], -1, 0
	s_cmpk_eq_i32 s9, 0xff
	s_cbranch_scc1 .LBB0_2
	s_and_b32 s3, s9, 15
	s_lshl_b32 s3, s3, 2
	s_load_dwordx2 s[76:77], s[10:11], s3 offset:0x0
	s_lshl_b32 s3, s9, 4
	s_add_i32 s9, s9, s2
	s_ashr_i32 s10, s2, 4
	s_and_b32 s89, s3, 0x7fffff00
	s_and_b32 s9, s9, 7
	s_waitcnt lgkmcnt(0)
	s_sub_i32 s3, s77, s76
	s_and_b32 s10, s10, -8
	s_or_b32 s91, s9, s10
	s_add_i32 s9, s3, 63
	s_ashr_i32 s10, s9, 31
	s_lshr_b32 s10, s10, 26
	s_add_i32 s9, s9, s10
	s_ashr_i32 s82, s9, 6
.LBB0_2:
	s_andn2_b64 vcc, exec, s[6:7]
	s_cbranch_vccnz .LBB0_66
	v_bfe_u32 v1, v0, 5, 1
	v_lshrrev_b32_e32 v2, 1, v0
	v_lshlrev_b32_e32 v4, 7, v0
	v_bfe_u32 v3, v0, 1, 3
	v_and_b32_e32 v4, 0xf80, v4
	v_bitop3_b32 v2, v1, v2, 7 bitop3:0x78
	v_lshl_or_b32 v230, v2, 4, v4
	v_bitop3_b32 v2, v1, v3, 2 bitop3:0x36
	v_lshl_or_b32 v231, v2, 4, v4
	v_bitop3_b32 v2, v1, v3, 4 bitop3:0x36
	v_lshl_or_b32 v232, v2, 4, v4
	v_bitop3_b32 v2, v1, v3, 6 bitop3:0x36
	v_lshlrev_b32_e32 v18, 4, v0
	v_lshl_or_b32 v233, v2, 4, v4
	v_lshlrev_b32_e32 v2, 1, v0
	v_lshlrev_b32_e32 v3, 3, v0
	v_and_b32_e32 v4, 0xc0, v18
	v_and_b32_e32 v2, 32, v2
	v_and_b32_e32 v3, 24, v3
	v_lshl_or_b32 v1, v1, 8, v4
	v_or3_b32 v234, v1, v2, v3
	v_mov_b32_e32 v3, 0
	s_lshr_b32 s6, s8, 6
	v_mov_b32_e32 v1, v3
	v_mov_b32_e32 v16, v3
	v_mov_b32_e32 v17, v3
	v_lshl_add_u64 v[226:227], s[4:5], 0, v[0:1]
	s_lshl_b32 s33, s6, 5
	s_waitcnt lgkmcnt(0)
	v_cmp_gt_u32_e64 s[34:35], 8, v0
	s_and_saveexec_b64 s[36:37], s[34:35]
	s_cbranch_execz .Lst_ub
	global_load_ubyte v162, v[226:227], off
